# baseline (speedup 1.0000x reference)
.LBB2_2:
	s_load_dword s3, s[0:1], 0x20
	s_load_dwordx2 s[8:9], s[0:1], 0x10
	s_and_b32 s10, s2, 7
	v_cvt_f32_ubyte0_e32 v3, s10
	v_lshrrev_b32_e32 v12, 4, v0
	s_waitcnt lgkmcnt(0)
	s_mul_hi_i32 s0, s3, 0x2aaaaaab
	s_lshr_b32 s1, s0, 31
	s_ashr_i32 s0, s0, 7
	s_add_i32 s3, s0, s1
	v_cvt_f32_i32_e32 v1, s3
	s_ashr_i32 s0, s3, 30
	s_or_b32 s11, s0, 1
	v_xor_b32_e32 v10, v12, v0
	v_rcp_iflag_f32_e32 v2, v1
	v_lshlrev_b32_e32 v149, 4, v0
	v_mov_b32_e32 v11, 0x60
	v_add_u32_e32 v14, 0, v149
	v_mul_f32_e32 v2, v3, v2
	v_trunc_f32_e32 v2, v2
	v_fma_f32 v3, -v2, v1, v3
	v_cvt_i32_f32_e32 v2, v2
	v_cmp_ge_f32_e64 s[0:1], |v3|, |v1|
	s_and_b64 s[0:1], s[0:1], exec
	s_cselect_b32 s0, s11, 0
	v_readfirstlane_b32 s1, v2
	s_add_i32 s1, s1, s0
	s_bfe_i32 s0, s1, 0x170000
	s_mul_i32 s0, s0, s3
	s_sub_i32 s0, s10, s0
	s_lshl_b32 s0, s0, 2
	s_lshr_b32 s3, s2, 6
	s_add_i32 s13, s0, s3
	s_lshl_b32 s0, s2, 5
	s_lshl_b32 s15, s1, 11
	s_and_b32 s18, s0, 0x700
	s_or_b32 s12, s15, s18
	v_lshrrev_b32_e32 v1, 3, v0
	v_or_b32_e32 v2, s12, v1
	s_mulk_i32 s13, 0xc0
	v_ashrrev_i32_e32 v3, 31, v2
	v_lshlrev_b64 v[4:5], 11, v[2:3]
	v_or_b32_e32 v2, s13, v1
	v_mov_b32_e32 v3, 0
	v_lshlrev_b64 v[6:7], 11, v[2:3]
	v_lshlrev_b32_e32 v2, 4, v10
	v_and_b32_e32 v10, 64, v0
	v_cmp_ne_u32_e32 vcc, 0, v10
	v_and_b32_e32 v143, 15, v0
	v_lshl_add_u64 v[4:5], s[4:5], 0, v[4:5]
	v_and_b32_e32 v2, 0x70, v2
	v_cndmask_b32_e32 v142, 0, v11, vcc
	v_readfirstlane_b32 s0, v14
	v_add_u32_e32 v16, 0x2000, v14
	v_lshl_add_u64 v[4:5], v[4:5], 0, v[2:3]
	v_or_b32_e32 v10, v142, v143
	s_mov_b32 m0, s0
	s_mov_b64 s[0:1], 0x20000
	v_readfirstlane_b32 s2, v16
	v_add_u32_e32 v16, 0x4000, v14
	v_lshlrev_b32_e32 v146, 7, v10
	global_load_lds_dwordx4 v[4:5], off
	v_lshl_add_u64 v[10:11], v[4:5], 0, s[0:1]
	s_mov_b32 m0, s2
	s_mov_b64 s[2:3], 0x40000
	v_readfirstlane_b32 s10, v16
	global_load_lds_dwordx4 v[10:11], off
	v_lshl_add_u64 v[10:11], v[4:5], 0, s[2:3]
	s_mov_b32 m0, s10
	s_mov_b64 s[10:11], 0x60000
	v_add_u32_e32 v16, 0x6000, v14
	v_lshl_add_u64 v[8:9], s[6:7], 0, v[6:7]
	v_add_u32_e32 v15, 0x8000, v14
	global_load_lds_dwordx4 v[10:11], off
	v_lshl_add_u64 v[10:11], v[4:5], 0, s[10:11]
	v_readfirstlane_b32 s10, v16
	v_lshl_add_u64 v[8:9], v[8:9], 0, v[2:3]
	s_mov_b32 m0, s10
	v_readfirstlane_b32 s10, v15
	v_add_u32_e32 v15, 0xa000, v14
	v_lshrrev_b32_e32 v2, 1, v0
	global_load_lds_dwordx4 v[10:11], off
	s_mov_b32 m0, s10
	v_lshl_add_u64 v[10:11], v[8:9], 0, s[0:1]
	v_readfirstlane_b32 s0, v15
	v_add_u32_e32 v15, 0xc000, v14
	v_bfe_u32 v145, v0, 4, 2
	v_and_b32_e32 v141, 0xc0, v2
	global_load_lds_dwordx4 v[8:9], off
	s_mov_b32 m0, s0
	v_readfirstlane_b32 s0, v15
	v_bitop3_b32 v13, v145, v2, 7 bitop3:0x78
	v_or_b32_e32 v2, v141, v143
	global_load_lds_dwordx4 v[10:11], off
	s_mov_b32 m0, s0
	s_add_i32 s0, 0, 0x16000
	v_add_u32_e32 v15, 0xe000, v14
	v_lshl_add_u64 v[10:11], v[8:9], 0, s[2:3]
	v_lshlrev_b32_e32 v147, 7, v2
	v_add_u32_e32 v2, s0, v149
	s_mov_b64 s[0:1], 0x80
	v_readfirstlane_b32 s2, v15
	v_add_u32_e32 v15, 0x10000, v14
	global_load_lds_dwordx4 v[10:11], off
	v_lshl_add_u64 v[10:11], v[4:5], 0, s[0:1]
	s_mov_b32 m0, s2
	s_mov_b64 s[2:3], 0x20080
	v_readfirstlane_b32 s10, v15
	v_add_u32_e32 v15, 0x12000, v14
	global_load_lds_dwordx4 v[10:11], off
	v_lshl_add_u64 v[10:11], v[4:5], 0, s[2:3]
	s_mov_b32 m0, s10
	s_mov_b64 s[10:11], 0x40080
	v_readfirstlane_b32 s16, v15
	global_load_lds_dwordx4 v[10:11], off
	v_lshl_add_u64 v[10:11], v[4:5], 0, s[10:11]
	s_mov_b32 m0, s16
	s_mov_b64 s[16:17], 0x60080
	global_load_lds_dwordx4 v[10:11], off
	v_add_u32_e32 v10, 0x14000, v14
	v_lshl_add_u64 v[4:5], v[4:5], 0, s[16:17]
	v_readfirstlane_b32 s16, v10
	s_mov_b32 m0, s16
	v_add_u32_e32 v10, 0x2000, v2
	global_load_lds_dwordx4 v[4:5], off
	v_lshl_add_u64 v[4:5], v[8:9], 0, s[0:1]
	v_readfirstlane_b32 s0, v2
	s_mov_b32 m0, s0
	v_readfirstlane_b32 s0, v10
	v_add_u32_e32 v2, 0x4000, v2
	global_load_lds_dwordx4 v[4:5], off
	v_lshl_add_u64 v[4:5], v[8:9], 0, s[2:3]
	s_mov_b32 m0, s0
	v_readfirstlane_b32 s0, v2
	global_load_lds_dwordx4 v[4:5], off
	v_lshl_add_u64 v[4:5], v[8:9], 0, s[10:11]
	s_mov_b32 m0, s0
	v_lshlrev_b32_e32 v2, 4, v13
	global_load_lds_dwordx4 v[4:5], off
	v_add3_u32 v150, 0, v147, v2
	v_add3_u32 v151, 0, v146, v2
	v_or_b32_e32 v1, s15, v1
	v_or_b32_e32 v4, s18, v1
	v_and_b32_e32 v140, 63, v0
	v_lshrrev_b32_e32 v144, 6, v0
	v_ashrrev_i32_e32 v5, 31, v4
	v_bitop3_b32 v0, v12, 7, v0 bitop3:0x48
	v_xor_b32_e32 v148, 64, v2
	v_lshlrev_b64 v[4:5], 11, v[4:5]
	v_lshlrev_b32_e32 v2, 4, v0
	v_or_b32_e32 v4, v4, v2
	v_or_b32_e32 v6, v6, v2
	s_mov_b32 s14, 0
	v_lshl_add_u64 v[0:1], s[4:5], 0, v[4:5]
	v_lshl_add_u64 v[138:139], s[6:7], 0, v[6:7]
	s_mov_b64 s[0:1], 0
	s_mov_b64 s[2:3], 0x100
	s_mov_b64 s[4:5], 0x20100
	s_mov_b64 s[6:7], 0x40100
	s_mov_b64 s[10:11], 0x60100
	v_lshl_add_u64 v[192:193], v[0:1], 0, s[2:3]
	v_lshl_add_u64 v[194:195], v[0:1], 0, s[4:5]
	v_lshl_add_u64 v[196:197], v[0:1], 0, s[6:7]
	v_lshl_add_u64 v[198:199], v[0:1], 0, s[10:11]
	v_lshl_add_u64 v[200:201], v[138:139], 0, s[2:3]
	v_lshl_add_u64 v[202:203], v[138:139], 0, s[4:5]
	v_lshl_add_u64 v[204:205], v[138:139], 0, s[6:7]
	v_readfirstlane_b32 s21, v149
	s_mov_b64 s[22:23], 0x80
	v_mov_b32_e32 v2, v3
	v_mov_b32_e32 v4, v3
	v_mov_b32_e32 v5, v3
	v_mov_b32_e32 v6, v3
	v_mov_b32_e32 v7, v3
	v_mov_b32_e32 v8, v3
	v_mov_b32_e32 v9, v3
	v_mov_b32_e32 v10, v3
	v_mov_b32_e32 v11, v3
	v_mov_b32_e32 v12, v3
	v_mov_b32_e32 v13, v3
	v_mov_b32_e32 v14, v3
	v_mov_b32_e32 v15, v3
	v_mov_b32_e32 v16, v3
	v_mov_b32_e32 v17, v3
	v_mov_b32_e32 v18, v3
	v_mov_b32_e32 v19, v3
	v_mov_b32_e32 v20, v3
	v_mov_b32_e32 v21, v3
	v_mov_b32_e32 v22, v3
	v_mov_b32_e32 v23, v3
	v_mov_b32_e32 v24, v3
	v_mov_b32_e32 v25, v3
	v_mov_b32_e32 v26, v3
	v_mov_b32_e32 v27, v3
	v_mov_b32_e32 v28, v3
	v_mov_b32_e32 v29, v3
	v_mov_b32_e32 v30, v3
	v_mov_b32_e32 v31, v3
	v_mov_b32_e32 v32, v3
	v_mov_b32_e32 v33, v3
	v_mov_b32_e32 v38, v3
	v_mov_b32_e32 v39, v3
	v_mov_b32_e32 v40, v3
	v_mov_b32_e32 v41, v3
	v_mov_b32_e32 v42, v3
	v_mov_b32_e32 v43, v3
	v_mov_b32_e32 v44, v3
	v_mov_b32_e32 v45, v3
	v_mov_b32_e32 v46, v3
	v_mov_b32_e32 v47, v3
	v_mov_b32_e32 v48, v3
	v_mov_b32_e32 v49, v3
	v_mov_b32_e32 v54, v3
	v_mov_b32_e32 v55, v3
	v_mov_b32_e32 v56, v3
	v_mov_b32_e32 v57, v3
	v_mov_b32_e32 v58, v3
	v_mov_b32_e32 v59, v3
	v_mov_b32_e32 v60, v3
	v_mov_b32_e32 v61, v3
	v_mov_b32_e32 v62, v3
	v_mov_b32_e32 v63, v3
	v_mov_b32_e32 v64, v3
	v_mov_b32_e32 v65, v3
	v_mov_b32_e32 v70, v3
	v_mov_b32_e32 v71, v3
	v_mov_b32_e32 v72, v3
	v_mov_b32_e32 v73, v3
	v_mov_b32_e32 v78, v3
	v_mov_b32_e32 v79, v3
	v_mov_b32_e32 v80, v3
	v_mov_b32_e32 v81, v3
	v_mov_b32_e32 v94, v3
	v_mov_b32_e32 v95, v3
	v_mov_b32_e32 v96, v3
	v_mov_b32_e32 v97, v3
	v_mov_b32_e32 v102, v3
	v_mov_b32_e32 v103, v3
	v_mov_b32_e32 v104, v3
	v_mov_b32_e32 v105, v3
	v_mov_b32_e32 v110, v3
	v_mov_b32_e32 v111, v3
	v_mov_b32_e32 v112, v3
	v_mov_b32_e32 v113, v3
	v_mov_b32_e32 v114, v3
	v_mov_b32_e32 v115, v3
	v_mov_b32_e32 v116, v3
	v_mov_b32_e32 v117, v3
	v_mov_b32_e32 v122, v3
	v_mov_b32_e32 v123, v3
	v_mov_b32_e32 v124, v3
	v_mov_b32_e32 v125, v3
	v_mov_b32_e32 v126, v3
	v_mov_b32_e32 v127, v3
	v_mov_b32_e32 v128, v3
	v_mov_b32_e32 v129, v3
	v_mov_b32_e32 v130, v3
	v_mov_b32_e32 v131, v3
	v_mov_b32_e32 v132, v3
	v_mov_b32_e32 v133, v3
	v_mov_b32_e32 v134, v3
	v_mov_b32_e32 v135, v3
	v_mov_b32_e32 v136, v3
	v_mov_b32_e32 v137, v3
	s_waitcnt vmcnt(7) lgkmcnt(0)
	s_barrier
	ds_read_b128 v[118:121], v150
	ds_read_b128 v[106:109], v150 offset:2048
	ds_read_b128 v[86:89], v150 offset:4096
	ds_read_b128 v[34:37], v150 offset:6144
	ds_read_b128 v[98:101], v151 offset:32768
	ds_read_b128 v[90:93], v151 offset:34816
	ds_read_b128 v[82:85], v151 offset:36864
	ds_read_b128 v[74:77], v151 offset:38912
	ds_read_b128 v[66:69], v151 offset:40960
	ds_read_b128 v[50:53], v151 offset:43008
